# P2 stage G: per-token scale reads issued in the MFMA shadow (free VGPRs, counted lgkmcnt); stacked on stage B pipelining
# baseline (speedup 1.0000x reference)
.LBB0_456:
	s_waitcnt lgkmcnt(0)
	s_barrier
	s_add_i32 s10, 0, 0x8000
	v_bfe_u32 v1, v186, 5, 1
	v_lshl_or_b32 v2, v1, 2, s4
	v_or_b32_e32 v211, 8, v2
	v_lshlrev_b32_e32 v4, 2, v2
	v_lshlrev_b32_e32 v8, 2, v211
	v_or_b32_e32 v214, 16, v2
	v_or_b32_e32 v216, 24, v2
	v_add_u32_e32 v5, s67, v4
	v_add_u32_e32 v6, s82, v4
	v_add_u32_e32 v4, s83, v4
	v_add_u32_e32 v9, s67, v8
	v_lshlrev_b32_e32 v12, 2, v214
	v_lshlrev_b32_e32 v16, 2, v216
	ds_read_b128 v[154:157], v5
	ds_read_b128 v[158:161], v6
	ds_read_b128 v[4:7], v4
	ds_read_b128 v[162:165], v9
	v_add_u32_e32 v9, s82, v8
	v_add_u32_e32 v8, s83, v8
	v_add_u32_e32 v13, s67, v12
	v_add_u32_e32 v14, s82, v12
	v_add_u32_e32 v12, s83, v12
	v_add_u32_e32 v17, s67, v16
	ds_read_b128 v[166:169], v9
	ds_read_b128 v[8:11], v8
	ds_read_b128 v[170:173], v13
	ds_read_b128 v[174:177], v14
	ds_read_b128 v[12:15], v12
	ds_read_b128 v[178:181], v17
	v_add_u32_e32 v17, s82, v16
	v_add_u32_e32 v16, s83, v16
	ds_read_b128 v[182:185], v17
	ds_read_b128 v[150:153], v16
	v_lshrrev_b32_e32 v16, 3, v186
	v_bfe_u32 v217, v186, 2, 2
	v_and_b32_e32 v16, 2, v16
	v_bfe_u32 v17, v186, 1, 1
	v_or3_b32 v218, v16, s5, v17
	v_lshlrev_b32_e32 v219, 2, v217
	v_lshlrev_b32_e32 v16, 3, v186
	v_and_or_b32 v220, v16, 8, s10
	v_bitop3_b32 v16, v219, v218, v1 bitop3:0x36
	v_or_b32_e32 v2, v2, v217
	v_lshl_add_u32 v215, v16, 4, v220
	v_lshl_add_u32 v2, v2, 8, v215
	ds_read_b64_tr_b16 v[16:17], v2
	v_or_b32_e32 v2, v211, v217
	v_bfe_u32 v211, v211, 2, 2
	v_bitop3_b32 v211, v211, v218, v219 bitop3:0x36
	v_lshlrev_b32_e32 v2, 8, v2
	v_lshlrev_b32_e32 v211, 4, v211
	v_add3_u32 v2, v2, v220, v211
	ds_read_b64_tr_b16 v[212:213], v2
	v_or_b32_e32 v2, v214, v217
	v_lshl_add_u32 v2, v2, 8, v215
	v_bfe_u32 v211, v216, 2, 2
	ds_read_b64_tr_b16 v[214:215], v2
	v_or_b32_e32 v2, v216, v217
	v_bitop3_b32 v211, v211, v218, v219 bitop3:0x36
	v_lshlrev_b32_e32 v2, 8, v2
	v_lshlrev_b32_e32 v211, 4, v211
	v_add3_u32 v2, v2, v220, v211
	ds_read_b64_tr_b16 v[216:217], v2
	s_waitcnt lgkmcnt(0)
	v_and_b32_e32 v219, 0xffff0000, v16
	v_lshlrev_b32_e32 v218, 16, v16
	s_waitcnt lgkmcnt(10)
	v_pk_fma_f32 v[66:67], v[66:67], v[158:159], v[218:219] neg_lo:[1,0,0] neg_hi:[1,0,0]
	v_and_or_b32 v2, v186, 31, s17
	v_pk_mul_f32 v[66:67], v[154:155], v[66:67]
	v_and_b32_e32 v155, 0xffff0000, v17
	v_lshlrev_b32_e32 v154, 16, v17
	v_pk_fma_f32 v[16:17], v[68:69], v[160:161], v[154:155] neg_lo:[1,0,0] neg_hi:[1,0,0]
	v_and_b32_e32 v69, 0xffff0000, v212
	v_lshlrev_b32_e32 v68, 16, v212
	v_lshlrev_b32_e32 v2, 7, v2
	v_lshlrev_b32_e32 v1, 3, v1
	v_pk_mul_f32 v[16:17], v[156:157], v[16:17]
	s_waitcnt lgkmcnt(7)
	v_pk_fma_f32 v[68:69], v[70:71], v[166:167], v[68:69] neg_lo:[1,0,0] neg_hi:[1,0,0]
	v_and_b32_e32 v71, 0xffff0000, v213
	v_lshlrev_b32_e32 v70, 16, v213
	v_add3_u32 v1, s18, v2, v1
	v_bitop3_b32 v2, v186, s40, 7 bitop3:0x6c
	v_pk_fma_f32 v[70:71], v[72:73], v[168:169], v[70:71] neg_lo:[1,0,0] neg_hi:[1,0,0]
	v_and_b32_e32 v73, 0xffff0000, v214
	v_lshlrev_b32_e32 v72, 16, v214
	v_cvt_pk_bf16_f32 v66, v66, v67
	v_cvt_pk_bf16_f32 v67, v16, v17
	v_lshl_add_u32 v2, v2, 4, v1
	v_pk_mul_f32 v[68:69], v[162:163], v[68:69]
	v_pk_mul_f32 v[70:71], v[164:165], v[70:71]
	s_waitcnt lgkmcnt(4)
	v_pk_fma_f32 v[72:73], v[74:75], v[174:175], v[72:73] neg_lo:[1,0,0] neg_hi:[1,0,0]
	v_and_b32_e32 v75, 0xffff0000, v215
	v_lshlrev_b32_e32 v74, 16, v215
	ds_write_b64 v2, v[66:67]
	v_bitop3_b32 v2, v186, s65, 7 bitop3:0x6c
	v_pk_fma_f32 v[74:75], v[76:77], v[176:177], v[74:75] neg_lo:[1,0,0] neg_hi:[1,0,0]
	v_and_b32_e32 v77, 0xffff0000, v216
	v_lshlrev_b32_e32 v76, 16, v216
	v_cvt_pk_bf16_f32 v16, v68, v69
	v_cvt_pk_bf16_f32 v17, v70, v71
	v_lshl_add_u32 v2, v2, 4, v1
	v_pk_mul_f32 v[72:73], v[170:171], v[72:73]
	v_pk_mul_f32 v[74:75], v[172:173], v[74:75]
	s_waitcnt lgkmcnt(2)
	v_pk_fma_f32 v[76:77], v[78:79], v[182:183], v[76:77] neg_lo:[1,0,0] neg_hi:[1,0,0]
	v_and_b32_e32 v79, 0xffff0000, v217
	v_lshlrev_b32_e32 v78, 16, v217
	ds_write_b64 v2, v[16:17]
	v_bitop3_b32 v2, v186, s33, 7 bitop3:0x6c
	v_pk_fma_f32 v[78:79], v[80:81], v[184:185], v[78:79] neg_lo:[1,0,0] neg_hi:[1,0,0]
	v_cvt_pk_bf16_f32 v16, v72, v73
	v_cvt_pk_bf16_f32 v17, v74, v75
	v_lshl_add_u32 v2, v2, 4, v1
	v_pk_mul_f32 v[76:77], v[178:179], v[76:77]
	v_pk_mul_f32 v[78:79], v[180:181], v[78:79]
	ds_write_b64 v2, v[16:17]
	v_bitop3_b32 v2, v186, s2, 7 bitop3:0x6c
	v_cvt_pk_bf16_f32 v16, v76, v77
	v_cvt_pk_bf16_f32 v17, v78, v79
	v_lshl_add_u32 v1, v2, 4, v1
	ds_write_b64 v1, v[16:17]
	s_waitcnt lgkmcnt(0)
	s_barrier
	s_nop 0
	v_and_b32_e32 v1, 31, v186
	v_lshrrev_b32_e32 v66, 5, v186
	v_and_b32_e32 v2, 7, v186
	v_lshl_add_u32 v154, v1, 7, s27
	v_or_b32_e32 v1, s17, v1
	v_lshlrev_b32_e32 v16, 7, v1
	v_bitop3_b32 v1, v66, v2, 1 bitop3:0x6c
	v_add_u32_e32 v155, s18, v16
	v_lshlrev_b32_e32 v1, 4, v1
	v_bfe_u32 v17, v186, 5, 1
	v_add_u32_e32 v66, v154, v1
	v_add_u32_e32 v1, v155, v1
	ds_read_b128 v[66:69], v66
	ds_read_b128 v[70:73], v1
	v_bitop3_b32 v1, v17, v2, 2 bitop3:0x36
	v_lshlrev_b32_e32 v1, 4, v1
	v_add_u32_e32 v74, v154, v1
	v_add_u32_e32 v1, v155, v1
	ds_read_b128 v[156:159], v74
	ds_read_b128 v[160:163], v1
	s_and_b64 vcc, exec, s[14:15]
	s_cbranch_vccnz .Lp2g_notb
	v_bitop3_b32 v1, v17, v2, 4 bitop3:0x36
	v_lshlrev_b32_e32 v1, 4, v1
	v_add_u32_e32 v252, v154, v1
	v_add_u32_e32 v1, v155, v1
	ds_read_b128 v[244:247], v252
	ds_read_b128 v[248:251], v1
	v_bitop3_b32 v1, v17, v2, 6 bitop3:0x36
	v_lshlrev_b32_e32 v1, 4, v1
	v_add_u32_e32 v252, v154, v1
	v_add_u32_e32 v1, v155, v1
	ds_read_b128 v[164:167], v252
	ds_read_b128 v[168:171], v1
	v_lshl_add_u32 v253, v17, 4, s35
	ds_read_b128 v[228:231], v253
	ds_read_b128 v[232:235], v253 offset:32
	ds_read_b128 v[236:239], v253 offset:64
	ds_read_b128 v[240:243], v253 offset:96
	s_waitcnt lgkmcnt(10)
	v_mfma_f32_32x32x16_bf16 v[66:81], v[66:69], v[70:73], 0
	s_waitcnt lgkmcnt(8)
	v_mfma_f32_32x32x16_bf16 v[66:81], v[156:159], v[160:163], v[66:81]
	s_waitcnt lgkmcnt(6)
	v_mfma_f32_32x32x16_bf16 v[66:81], v[244:247], v[248:251], v[66:81]
	s_waitcnt lgkmcnt(4)
	v_mfma_f32_32x32x16_bf16 v[66:81], v[164:167], v[168:171], v[66:81]
	s_branch .LBB0_458
.Lp2g_notb:
	v_lshl_add_u32 v253, v17, 4, s35
	ds_read_b128 v[228:231], v253
	ds_read_b128 v[232:235], v253 offset:32
	ds_read_b128 v[236:239], v253 offset:64
	ds_read_b128 v[240:243], v253 offset:96
	s_waitcnt lgkmcnt(6)
	v_mfma_f32_32x32x16_bf16 v[66:81], v[66:69], v[70:73], 0
	s_waitcnt lgkmcnt(4)
	v_mfma_f32_32x32x16_bf16 v[66:81], v[156:159], v[160:163], v[66:81]
.LBB0_458:
	v_lshlrev_b32_e32 v1, 3, v17
	s_waitcnt lgkmcnt(3)
	s_nop 5
	s_nop 4
	v_pk_mul_f32 v[228:229], v[66:67], v[228:229]
	v_pk_mul_f32 v[230:231], v[68:69], v[230:231]
	v_cvt_pk_bf16_f32 v66, v66, v67
	v_cvt_pk_bf16_f32 v67, v68, v69
	v_xor_b32_e32 v68, s40, v2
	v_add_u32_e32 v17, 0, v1
	s_add_i32 s10, 0, 0x1c000
	v_lshl_add_u32 v68, v68, 4, v16
	v_add_u32_e32 v1, s10, v1
	v_add_u32_e32 v69, v17, v68
	ds_write_b64 v69, v[66:67] offset:16384
	v_cvt_pk_bf16_f32 v66, v228, v229
	v_cvt_pk_bf16_f32 v67, v230, v231
	v_add_u32_e32 v68, v1, v68
	ds_write_b64 v68, v[66:67]
	s_waitcnt lgkmcnt(4)
	v_pk_mul_f32 v[66:67], v[70:71], v[232:233]
	v_pk_mul_f32 v[68:69], v[72:73], v[234:235]
	v_cvt_pk_bf16_f32 v70, v70, v71
	v_cvt_pk_bf16_f32 v71, v72, v73
	v_xor_b32_e32 v72, s65, v2
	v_lshl_add_u32 v72, v72, 4, v16
	v_add_u32_e32 v73, v17, v72
	v_cvt_pk_bf16_f32 v66, v66, v67
	v_cvt_pk_bf16_f32 v67, v68, v69
	v_add_u32_e32 v68, v1, v72
	v_xor_b32_e32 v72, s33, v2
	ds_write_b64 v68, v[66:67]
	s_waitcnt lgkmcnt(4)
	v_pk_mul_f32 v[66:67], v[74:75], v[236:237]
	v_pk_mul_f32 v[68:69], v[76:77], v[238:239]
	v_lshl_add_u32 v72, v72, 4, v16
	v_xor_b32_e32 v2, s2, v2
	ds_write_b64 v73, v[70:71] offset:16384
	v_cvt_pk_bf16_f32 v70, v74, v75
	v_cvt_pk_bf16_f32 v71, v76, v77
	v_add_u32_e32 v73, v17, v72
	v_cvt_pk_bf16_f32 v66, v66, v67
	v_cvt_pk_bf16_f32 v67, v68, v69
	v_add_u32_e32 v68, v1, v72
	v_lshl_add_u32 v2, v2, 4, v16
	ds_write_b64 v73, v[70:71] offset:16384
	ds_write_b64 v68, v[66:67]
	s_waitcnt lgkmcnt(6)
	v_pk_mul_f32 v[66:67], v[78:79], v[240:241]
	v_pk_mul_f32 v[68:69], v[80:81], v[242:243]
	v_cvt_pk_bf16_f32 v70, v78, v79
	v_cvt_pk_bf16_f32 v71, v80, v81
	v_add_u32_e32 v16, v17, v2
	ds_write_b64 v16, v[70:71] offset:16384
	v_cvt_pk_bf16_f32 v16, v66, v67
	v_cvt_pk_bf16_f32 v17, v68, v69
	v_add_u32_e32 v1, v1, v2
	ds_write_b64 v1, v[16:17]
	s_waitcnt lgkmcnt(0)
	s_barrier
	v_pk_mul_f32 v[52:53], v[52:53], v[6:7]
	v_and_b32_e32 v1, 31, v186
	v_lshrrev_b32_e32 v68, 5, v186
	v_and_b32_e32 v67, 7, v186
	v_lshl_add_u32 v17, v1, 7, s34
	v_or_b32_e32 v16, s17, v1
	v_bitop3_b32 v1, v68, v67, 1 bitop3:0x6c
	v_lshl_add_u32 v66, v16, 7, 0
	v_lshlrev_b32_e32 v1, 4, v1
	v_bfe_u32 v2, v186, 5, 1
	v_add_u32_e32 v6, v17, v1
	v_add_u32_e32 v1, v66, v1
	ds_read_b128 v[68:71], v6
	ds_read_b128 v[72:75], v1 offset:16384
	v_bitop3_b32 v1, v2, v67, 2 bitop3:0x36
	v_lshlrev_b32_e32 v1, 4, v1
	v_add_u32_e32 v6, v17, v1
	v_pk_mul_f32 v[64:65], v[64:65], v[152:153]
	v_add_u32_e32 v1, v66, v1
	ds_read_b128 v[76:79], v6
	ds_read_b128 v[152:155], v1 offset:16384
	v_pk_mul_f32 v[60:61], v[60:61], v[14:15]
	v_pk_mul_f32 v[56:57], v[56:57], v[10:11]
	v_pk_mul_f32 v[50:51], v[50:51], v[4:5]
	v_pk_mul_f32 v[62:63], v[62:63], v[150:151]
	v_pk_mul_f32 v[58:59], v[58:59], v[12:13]
	v_pk_mul_f32 v[54:55], v[54:55], v[8:9]
	s_and_b64 vcc, exec, s[14:15]
	s_cbranch_vccnz .Lp2h_notb
	v_bitop3_b32 v1, v2, v67, 4 bitop3:0x36
	v_lshlrev_b32_e32 v1, 4, v1
	v_add_u32_e32 v252, v17, v1
	v_add_u32_e32 v1, v66, v1
	ds_read_b128 v[4:7], v252
	ds_read_b128 v[8:11], v1 offset:16384
	v_bitop3_b32 v1, v2, v67, 6 bitop3:0x36
	v_lshlrev_b32_e32 v1, 4, v1
	v_add_u32_e32 v252, v17, v1
	v_add_u32_e32 v1, v66, v1
	ds_read_b128 v[12:15], v252
	ds_read_b128 v[244:247], v1 offset:16384
	s_waitcnt lgkmcnt(6)
	s_nop 0
	v_mfma_f32_32x32x16_bf16 v[50:65], v[68:71], v[72:75], v[50:65]
	s_waitcnt lgkmcnt(4)
	v_mfma_f32_32x32x16_bf16 v[50:65], v[76:79], v[152:155], v[50:65]
	s_waitcnt lgkmcnt(2)
	v_mfma_f32_32x32x16_bf16 v[50:65], v[4:7], v[8:11], v[50:65]
	s_waitcnt lgkmcnt(0)
	v_mfma_f32_32x32x16_bf16 v[50:65], v[12:15], v[244:247], v[50:65]
	s_branch .LBB0_372
